# MoE down-projection tile body on LDS-DMA staging as well
# speedup vs baseline: 1.0452x; 1.0058x over previous
;     ...
;     for (int i = 0; i < 4; ++i) ao[i] = arow((tid >> 3) + 32 * i) + (tid & 7) * 8;
;     const int bk = tid >> 4, bnc = tid & 15;
;     constexpr int NRB = B_F32 ? 8 : 4;
;     u32x4 ra0[4], ra1[4]; u32x4 rb0[NRB], rb1[NRB];
;     auto gloadA = [&](int kt, u32x4 (&ra)[4]) __attribute__((always_inline)) {
; #pragma unroll
;         for (int i = 0; i < 4; ++i) ra[i] = *(const u32x4*)(Abase + (ao[i] + kt * 64));
;     };
;     auto gloadB = [&](int kt, u32x4 (&rb)[NRB]) __attribute__((always_inline)) {
;         if (B_F32) {
;             const float* bp = (const float*)Bbase + (boff + (unsigned)((kt * 64 + bk) * ldb));
; #pragma unroll
;             for (int i = 0; i < 4; ++i) {
;                 if (bval) { rb[2 * i] = *(const u32x4*)(bp + (unsigned)(16 * i * ldb)); rb[2 * i + 1] = *(const u32x4*)(bp + (unsigned)(16 * i * ldb) + 4); }
;                 else { rb[2 * i] = (u32x4){0u, 0u, 0u, 0u}; rb[2 * i + 1] = rb[2 * i]; }
;             }
;         } else {
;             const bf16* bp = (const bf16*)Bbase + (boff + (unsigned)((kt * 64 + bk) * ldb));
; #pragma unroll
;             for (int i = 0; i < 4; ++i) rb[i] = bval ? *(const u32x4*)(bp + (unsigned)(16 * i * ldb)) : (u32x4){0u, 0u, 0u, 0u};
;         }
;     };
;     auto lstore = [&](const u32x4 (&ra)[4], const u32x4 (&rb)[NRB]) __attribute__((always_inline)) {
; #pragma unroll
;         for (int i = 0; i < 4; ++i) { const int row = (tid >> 3) + 32 * i, kc = tid & 7;
;             const u32x4 v = (kc & 1) ? (u32x4){ra[i][2], ra[i][3], ra[i][0], ra[i][1]} : ra[i];
;             *(u32x4*)(lds + (kc >> 2) * GA_KH + row * 64 + (kc & 3) * 16) = v; }
; #pragma unroll
;         for (int i = 0; i < 4; ++i) { const int k = bk + 16 * i;
;             u32x4 v;
;             if (B_F32) { const f32x4 x = __builtin_bit_cast(f32x4, rb[2 * i]), y = __builtin_bit_cast(f32x4, rb[2 * i + 1]);
;                 v[0] = pk2bf(x[0], x[1]); v[1] = pk2bf(x[2], x[3]); v[2] = pk2bf(y[0], y[1]); v[3] = pk2bf(y[2], y[3]); }
;             else v = rb[i];
;             *(u32x4*)(lds + GB_OFF + k * GB_ST + bnc * 16) = v; }
;     };
;     const lds_cptr la = (lds_cptr)lds + (wr * 64 + fr) * 64 + fq * 16;
;     const lds_cptr lb = (lds_cptr)lds + GB_OFF + (8 * fq + (fr >> 2) + (fq & 1) * 4) * GB_ST + wc * 128 + (fr & 3) * 8;
;     const int bsw = (fq & 1) ? -4 * GB_ST : 4 * GB_ST;
.LBB0_152:
	s_or_b64 exec, exec, s[28:29]
	s_waitcnt lgkmcnt(0)
	s_lshl_b64 s[16:17], s[72:73], 10
	s_add_u32 s28, s42, s16
	s_addc_u32 s29, s43, s17
	s_add_u32 s28, s28, 0xb3c6000
	s_addc_u32 s29, s29, 0
	s_lshl_b32 s7, s7, 20
	s_lshl_b32 s6, s59, 8
	s_and_b32 s6, s6, 0x700
	s_add_u32 s44, s42, s7
	s_addc_u32 s45, s43, 0
	s_add_u32 s44, s44, s6
	s_addc_u32 s45, s45, 0
	s_add_u32 s44, s44, 0x1cdd5100
	s_addc_u32 s45, s45, 0
	v_lshrrev_b32_e32 v211, 7, v118
	v_lshlrev_b32_e32 v211, 6, v211
	v_and_b32_e32 v215, 15, v118
	v_or_b32_e32 v211, v211, v215
	v_lshlrev_b32_e32 v211, 6, v211
	v_bfe_u32 v215, v118, 4, 2
	v_lshlrev_b32_e32 v215, 4, v215
	v_or_b32_e32 v211, v211, v215
	v_lshrrev_b32_e32 v215, 6, v118
	v_lshlrev_b32_e32 v215, 5, v215
	v_bfe_u32 v216, v118, 2, 4
	v_add_u32_e32 v215, v215, v216
	v_mul_u32_u24_e32 v215, 0x400, v215
	v_bfe_u32 v216, v118, 4, 2
	v_sub_u32_e32 v216, 0, v216
	v_and_b32_e32 v216, 3, v216
	v_and_b32_e32 v68, 3, v118
	v_xor_b32_e32 v216, v216, v68
	v_lshl_add_u32 v202, v216, 4, v215
	v_add_u32_e32 v203, 64, v202
	v_add_u32_e32 v204, 0x4000, v202
	v_add_u32_e32 v205, 64, v204
	v_lshrrev_b32_e32 v215, 6, v118
	v_lshlrev_b32_e32 v215, 4, v215
	v_bfe_u32 v216, v118, 4, 2
	v_add_u32_e32 v215, v215, v216
	v_mul_u32_u24_e32 v215, 0x800, v215
	v_bfe_u32 v68, v118, 1, 3
	v_xor_b32_e32 v68, v68, v216
	v_lshlrev_b32_e32 v68, 1, v68
	v_and_b32_e32 v216, 1, v118
	v_or_b32_e32 v68, v68, v216
	v_lshl_add_u32 v206, v68, 4, v215
	v_add_u32_e32 v207, 0x2000, v206
	v_xor_b32_e32 v68, 8, v68
	v_lshl_add_u32 v208, v68, 4, v215
	v_add_u32_e32 v208, 0x4000, v208
	v_add_u32_e32 v209, 0x2000, v208
	v_bfe_u32 v215, v118, 2, 2
	v_sub_u32_e32 v215, 0, v215
	v_and_b32_e32 v215, 3, v215
	v_lshlrev_b32_e32 v215, 4, v215
	v_xor_b32_e32 v211, v211, v215
	v_bfe_u32 v215, v118, 4, 2
	v_lshlrev_b32_e32 v215, 3, v215
	v_bfe_u32 v216, v118, 2, 2
	v_add_u32_e32 v215, v215, v216
	v_lshlrev_b32_e32 v215, 8, v215
	v_lshrrev_b32_e32 v68, 6, v118
	v_lshrrev_b32_e32 v210, 4, v118
	v_xor_b32_e32 v68, v68, v210
	v_and_b32_e32 v68, 1, v68
	v_lshlrev_b32_e32 v68, 7, v68
	v_or_b32_e32 v215, v215, v68
	v_and_b32_e32 v68, 3, v118
	v_lshlrev_b32_e32 v68, 3, v68
	v_or_b32_e32 v215, v215, v68
	v_xor_b32_e32 v68, 0, v216
	v_lshl_or_b32 v210, v68, 5, v215
	v_xor_b32_e32 v68, 1, v216
	v_lshl_or_b32 v212, v68, 5, v215
	v_xor_b32_e32 v68, 2, v216
	v_lshl_or_b32 v213, v68, 5, v215
	v_xor_b32_e32 v68, 3, v216
	v_lshl_or_b32 v214, v68, 5, v215
	v_lshrrev_b32_e32 v215, 6, v118
	s_nop 1
	v_readfirstlane_b32 s98, v215
	s_nop 1
	s_lshl_b32 s99, s98, 12
	s_lshl_b32 s98, s98, 11
	s_barrier
	s_add_u32 m0, s98, 0x0
	s_nop 0
	global_load_lds_dwordx4 v202, s[28:29]
	s_add_u32 m0, s98, 0x2040
	s_nop 0
	global_load_lds_dwordx4 v203, s[28:29]
	s_add_u32 m0, s98, 0x400
	s_nop 0
	global_load_lds_dwordx4 v204, s[28:29]
	s_add_u32 m0, s98, 0x2440
	s_nop 0
	global_load_lds_dwordx4 v205, s[28:29]
	s_add_u32 m0, s99, 0x4080
	s_nop 0
	global_load_lds_dwordx4 v206, s[44:45]
	s_add_u32 m0, s99, 0x4480
	s_nop 0
	global_load_lds_dwordx4 v207, s[44:45]
	s_add_u32 m0, s99, 0x4880
	s_nop 0
	global_load_lds_dwordx4 v208, s[44:45]
	s_add_u32 m0, s99, 0x4c80
	s_nop 0
	global_load_lds_dwordx4 v209, s[44:45]
	s_add_u32 s28, s28, 0x80
	s_addc_u32 s29, s29, 0
	s_add_u32 s44, s44, 0x20000
	s_addc_u32 s45, s45, 0
	v_mov_b32_e32 v4, 0
	v_mov_b32_e32 v5, 0
	v_mov_b32_e32 v6, 0
	v_mov_b32_e32 v7, 0
	v_mov_b32_e32 v8, 0
	v_mov_b32_e32 v9, 0
	v_mov_b32_e32 v10, 0
	v_mov_b32_e32 v11, 0
	v_mov_b32_e32 v12, 0
	v_mov_b32_e32 v13, 0
	v_mov_b32_e32 v14, 0
	v_mov_b32_e32 v15, 0
	v_mov_b32_e32 v16, 0
	v_mov_b32_e32 v17, 0
	v_mov_b32_e32 v18, 0
	v_mov_b32_e32 v19, 0
	v_mov_b32_e32 v20, 0
	v_mov_b32_e32 v21, 0
	v_mov_b32_e32 v22, 0
	v_mov_b32_e32 v23, 0
	v_mov_b32_e32 v24, 0
	v_mov_b32_e32 v25, 0
	v_mov_b32_e32 v26, 0
	v_mov_b32_e32 v27, 0
	v_mov_b32_e32 v28, 0
	v_mov_b32_e32 v29, 0
	v_mov_b32_e32 v30, 0
	v_mov_b32_e32 v31, 0
	v_mov_b32_e32 v32, 0
	v_mov_b32_e32 v33, 0
	v_mov_b32_e32 v34, 0
	v_mov_b32_e32 v35, 0
	v_mov_b32_e32 v36, 0
	v_mov_b32_e32 v37, 0
	v_mov_b32_e32 v38, 0
	v_mov_b32_e32 v39, 0
	v_mov_b32_e32 v40, 0
	v_mov_b32_e32 v41, 0
	v_mov_b32_e32 v42, 0
	v_mov_b32_e32 v43, 0
	v_mov_b32_e32 v44, 0
	v_mov_b32_e32 v45, 0
	v_mov_b32_e32 v46, 0
	v_mov_b32_e32 v47, 0
	v_mov_b32_e32 v48, 0
	v_mov_b32_e32 v49, 0
	v_mov_b32_e32 v50, 0
	v_mov_b32_e32 v51, 0
	v_mov_b32_e32 v52, 0
	v_mov_b32_e32 v53, 0
	v_mov_b32_e32 v54, 0
	v_mov_b32_e32 v55, 0
	v_mov_b32_e32 v56, 0
	v_mov_b32_e32 v57, 0
	v_mov_b32_e32 v58, 0
	v_mov_b32_e32 v59, 0
	v_mov_b32_e32 v60, 0
	v_mov_b32_e32 v61, 0
	v_mov_b32_e32 v62, 0
	v_mov_b32_e32 v63, 0
	v_mov_b32_e32 v64, 0
	v_mov_b32_e32 v65, 0
	v_mov_b32_e32 v66, 0
	v_mov_b32_e32 v67, 0
	s_mov_b32 s6, 0
	s_waitcnt vmcnt(0)
	s_barrier
; #define LAS __attribute__((address_space(3)))
; __device__ __forceinline__ s16x4 lds_tr(lds_cptr p) { return __builtin_bit_cast(s16x4, __builtin_amdgcn_ds_read_tr16_b64_v4i16((LAS s16x4*)p)); }
;     ...
;     auto compute = [&]() __attribute__((always_inline)) {
; #pragma unroll
;         for (int kh = 0; kh < 2; ++kh) {
;             bf16x8 af[4], bfr[4];
; #pragma unroll
;             for (int m = 0; m < 4; ++m) af[m] = *(const LAS bf16x8*)(la + kh * GA_KH + m * 1024);
; #pragma unroll
;             for (int n = 0; n < 4; ++n) {
;                 const s16x4 r0 = lds_tr(lb + kh * 32 * GB_ST + n * 32), r1 = lds_tr(lb + kh * 32 * GB_ST + n * 32 + bsw);
;                 bfr[n] = (bf16x8){r0[0], r0[1], r0[2], r0[3], r1[0], r1[1], r1[2], r1[3]};
;             }
; #pragma unroll
;             for (int m = 0; m < 4; ++m)
; #pragma unroll
;                 for (int n = 0; n < 4; ++n) acc[m][n] = __builtin_amdgcn_mfma_f32_16x16x32_bf16(bfr[n], af[m], acc[m][n], 0, 0, 0);
;         }
;     };
;     ...
;     gloadB(0, rb0); gloadA(0, ra0); gloadB(1, rb1);
;     for (int kt = 0; kt < nk; kt += 2) {
;         __syncthreads();
;         lstore(ra0, rb0);
;         __syncthreads();
;         gloadA(kt + 1, ra0);
;         if (kt + 2 < nk) gloadB(kt + 2, rb0);
;         compute();
;         __syncthreads();
;         lstore(ra0, rb1);
;         __syncthreads();
;         if (kt + 2 < nk) gloadA(kt + 2, ra0);
;         if (kt + 3 < nk) gloadB(kt + 3, rb1);
;         compute();
;     }
.Lm2_loop:
	s_add_u32 m0, s98, 0x9000
	ds_read_b64_tr_b16 v[166:167], v210 offset:16512
	ds_read_b64_tr_b16 v[168:169], v210 offset:17536
	ds_read_b128 v[136:139], v211
	ds_read_b64_tr_b16 v[170:171], v212 offset:16512
	ds_read_b64_tr_b16 v[172:173], v212 offset:17536
	s_waitcnt lgkmcnt(2)
	v_mfma_f32_16x16x32_bf16 v[4:7], v[166:169], v[136:139], v[4:7]
	global_load_lds_dwordx4 v202, s[28:29]
	s_add_u32 m0, s98, 0xb040
	ds_read_b64_tr_b16 v[174:175], v213 offset:16512
	ds_read_b64_tr_b16 v[176:177], v213 offset:17536
	s_waitcnt lgkmcnt(2)
	v_mfma_f32_16x16x32_bf16 v[8:11], v[170:173], v[136:139], v[8:11]
	global_load_lds_dwordx4 v203, s[28:29]
	s_add_u32 m0, s98, 0x9400
	ds_read_b64_tr_b16 v[178:179], v214 offset:16512
	ds_read_b64_tr_b16 v[180:181], v214 offset:17536
	s_waitcnt lgkmcnt(2)
	v_mfma_f32_16x16x32_bf16 v[12:15], v[174:177], v[136:139], v[12:15]
	global_load_lds_dwordx4 v204, s[28:29]
	s_add_u32 m0, s98, 0xb440
	ds_read_b128 v[140:143], v211 offset:1024
	s_waitcnt lgkmcnt(1)
	v_mfma_f32_16x16x32_bf16 v[16:19], v[178:181], v[136:139], v[16:19]
	global_load_lds_dwordx4 v205, s[28:29]
	s_add_u32 m0, s99, 0xd080
	ds_read_b128 v[158:161], v211 offset:2048
	s_waitcnt lgkmcnt(1)
	v_mfma_f32_16x16x32_bf16 v[20:23], v[166:169], v[140:143], v[20:23]
	global_load_lds_dwordx4 v206, s[44:45]
	s_add_u32 m0, s99, 0xd480
	ds_read_b128 v[162:165], v211 offset:3072
	v_mfma_f32_16x16x32_bf16 v[24:27], v[170:173], v[140:143], v[24:27]
	global_load_lds_dwordx4 v207, s[44:45]
	s_add_u32 m0, s99, 0xd880
	ds_read_b64_tr_b16 v[182:183], v210 offset:24704
	ds_read_b64_tr_b16 v[184:185], v210 offset:25728
	v_mfma_f32_16x16x32_bf16 v[28:31], v[174:177], v[140:143], v[28:31]
	global_load_lds_dwordx4 v208, s[44:45]
	s_add_u32 m0, s99, 0xdc80
	ds_read_b64_tr_b16 v[186:187], v212 offset:24704
	ds_read_b64_tr_b16 v[188:189], v212 offset:25728
	v_mfma_f32_16x16x32_bf16 v[32:35], v[178:181], v[140:143], v[32:35]
	global_load_lds_dwordx4 v209, s[44:45]
	s_add_u32 s28, s28, 0x80
	s_addc_u32 s29, s29, 0
	s_add_u32 s44, s44, 0x20000
	s_addc_u32 s45, s45, 0
	ds_read_b128 v[136:139], v211 offset:8256
	s_waitcnt lgkmcnt(6)
	v_mfma_f32_16x16x32_bf16 v[36:39], v[166:169], v[158:161], v[36:39]
	ds_read_b64_tr_b16 v[190:191], v213 offset:24704
	ds_read_b64_tr_b16 v[192:193], v213 offset:25728
	v_mfma_f32_16x16x32_bf16 v[40:43], v[170:173], v[158:161], v[40:43]
	ds_read_b64_tr_b16 v[198:199], v214 offset:24704
	ds_read_b64_tr_b16 v[200:201], v214 offset:25728
	v_mfma_f32_16x16x32_bf16 v[44:47], v[174:177], v[158:161], v[44:47]
	v_mfma_f32_16x16x32_bf16 v[48:51], v[178:181], v[158:161], v[48:51]
	ds_read_b128 v[140:143], v211 offset:9280
	s_waitcnt lgkmcnt(10)
	v_mfma_f32_16x16x32_bf16 v[52:55], v[166:169], v[162:165], v[52:55]
	v_mfma_f32_16x16x32_bf16 v[56:59], v[170:173], v[162:165], v[56:59]
	v_mfma_f32_16x16x32_bf16 v[60:63], v[174:177], v[162:165], v[60:63]
	v_mfma_f32_16x16x32_bf16 v[64:67], v[178:181], v[162:165], v[64:67]
	ds_read_b128 v[158:161], v211 offset:10304
	s_waitcnt lgkmcnt(6)
	v_mfma_f32_16x16x32_bf16 v[4:7], v[182:185], v[136:139], v[4:7]
	v_mfma_f32_16x16x32_bf16 v[8:11], v[186:189], v[136:139], v[8:11]
	s_waitcnt lgkmcnt(4)
	v_mfma_f32_16x16x32_bf16 v[12:15], v[190:193], v[136:139], v[12:15]
	s_waitcnt lgkmcnt(2)
	v_mfma_f32_16x16x32_bf16 v[16:19], v[198:201], v[136:139], v[16:19]
	ds_read_b128 v[162:165], v211 offset:11328
	s_waitcnt lgkmcnt(2)
	v_mfma_f32_16x16x32_bf16 v[20:23], v[182:185], v[140:143], v[20:23]
	v_mfma_f32_16x16x32_bf16 v[24:27], v[186:189], v[140:143], v[24:27]
	v_mfma_f32_16x16x32_bf16 v[28:31], v[190:193], v[140:143], v[28:31]
	v_mfma_f32_16x16x32_bf16 v[32:35], v[198:201], v[140:143], v[32:35]
	s_waitcnt lgkmcnt(1)
	v_mfma_f32_16x16x32_bf16 v[36:39], v[182:185], v[158:161], v[36:39]
	v_mfma_f32_16x16x32_bf16 v[40:43], v[186:189], v[158:161], v[40:43]
	v_mfma_f32_16x16x32_bf16 v[44:47], v[190:193], v[158:161], v[44:47]
	v_mfma_f32_16x16x32_bf16 v[48:51], v[198:201], v[158:161], v[48:51]
	s_waitcnt lgkmcnt(0)
	v_mfma_f32_16x16x32_bf16 v[52:55], v[182:185], v[162:165], v[52:55]
	v_mfma_f32_16x16x32_bf16 v[56:59], v[186:189], v[162:165], v[56:59]
	v_mfma_f32_16x16x32_bf16 v[60:63], v[190:193], v[162:165], v[60:63]
	v_mfma_f32_16x16x32_bf16 v[64:67], v[198:201], v[162:165], v[64:67]
	s_waitcnt vmcnt(0) lgkmcnt(0)
	s_barrier
; #define LAS __attribute__((address_space(3)))
; __device__ __forceinline__ s16x4 lds_tr(lds_cptr p) { return __builtin_bit_cast(s16x4, __builtin_amdgcn_ds_read_tr16_b64_v4i16((LAS s16x4*)p)); }
;     ...
;     auto compute = [&]() __attribute__((always_inline)) {
; #pragma unroll
;         for (int kh = 0; kh < 2; ++kh) {
;             bf16x8 af[4], bfr[4];
; #pragma unroll
;             for (int m = 0; m < 4; ++m) af[m] = *(const LAS bf16x8*)(la + kh * GA_KH + m * 1024);
; #pragma unroll
;             for (int n = 0; n < 4; ++n) {
;                 const s16x4 r0 = lds_tr(lb + kh * 32 * GB_ST + n * 32), r1 = lds_tr(lb + kh * 32 * GB_ST + n * 32 + bsw);
;                 bfr[n] = (bf16x8){r0[0], r0[1], r0[2], r0[3], r1[0], r1[1], r1[2], r1[3]};
;             }
; #pragma unroll
;             for (int m = 0; m < 4; ++m)
; #pragma unroll
;                 for (int n = 0; n < 4; ++n) acc[m][n] = __builtin_amdgcn_mfma_f32_16x16x32_bf16(bfr[n], af[m], acc[m][n], 0, 0, 0);
;         }
;     };
;     ...
;     gloadB(0, rb0); gloadA(0, ra0); gloadB(1, rb1);
;     for (int kt = 0; kt < nk; kt += 2) {
;         __syncthreads();
;         lstore(ra0, rb0);
;         __syncthreads();
;         gloadA(kt + 1, ra0);
;         if (kt + 2 < nk) gloadB(kt + 2, rb0);
;         compute();
;         __syncthreads();
;         lstore(ra0, rb1);
;         __syncthreads();
;         if (kt + 2 < nk) gloadA(kt + 2, ra0);
;         if (kt + 3 < nk) gloadB(kt + 3, rb1);
;         compute();
;     }
	s_add_u32 m0, s98, 0x0
	ds_read_b64_tr_b16 v[166:167], v210 offset:53376
	ds_read_b64_tr_b16 v[168:169], v210 offset:54400
	ds_read_b128 v[136:139], v211 offset:36864
	ds_read_b64_tr_b16 v[170:171], v212 offset:53376
	ds_read_b64_tr_b16 v[172:173], v212 offset:54400
	s_waitcnt lgkmcnt(2)
	v_mfma_f32_16x16x32_bf16 v[4:7], v[166:169], v[136:139], v[4:7]
	global_load_lds_dwordx4 v202, s[28:29]
	s_add_u32 m0, s98, 0x2040
	ds_read_b64_tr_b16 v[174:175], v213 offset:53376
	ds_read_b64_tr_b16 v[176:177], v213 offset:54400
	s_waitcnt lgkmcnt(2)
	v_mfma_f32_16x16x32_bf16 v[8:11], v[170:173], v[136:139], v[8:11]
	global_load_lds_dwordx4 v203, s[28:29]
	s_add_u32 m0, s98, 0x400
	ds_read_b64_tr_b16 v[178:179], v214 offset:53376
	ds_read_b64_tr_b16 v[180:181], v214 offset:54400
	s_waitcnt lgkmcnt(2)
	v_mfma_f32_16x16x32_bf16 v[12:15], v[174:177], v[136:139], v[12:15]
	global_load_lds_dwordx4 v204, s[28:29]
	s_add_u32 m0, s98, 0x2440
	ds_read_b128 v[140:143], v211 offset:37888
	s_waitcnt lgkmcnt(1)
	v_mfma_f32_16x16x32_bf16 v[16:19], v[178:181], v[136:139], v[16:19]
	global_load_lds_dwordx4 v205, s[28:29]
	s_add_u32 m0, s99, 0x4080
	ds_read_b128 v[158:161], v211 offset:38912
	s_waitcnt lgkmcnt(1)
	v_mfma_f32_16x16x32_bf16 v[20:23], v[166:169], v[140:143], v[20:23]
	global_load_lds_dwordx4 v206, s[44:45]
	s_add_u32 m0, s99, 0x4480
	ds_read_b128 v[162:165], v211 offset:39936
	v_mfma_f32_16x16x32_bf16 v[24:27], v[170:173], v[140:143], v[24:27]
	global_load_lds_dwordx4 v207, s[44:45]
	s_add_u32 m0, s99, 0x4880
	ds_read_b64_tr_b16 v[182:183], v210 offset:61568
	ds_read_b64_tr_b16 v[184:185], v210 offset:62592
	v_mfma_f32_16x16x32_bf16 v[28:31], v[174:177], v[140:143], v[28:31]
	global_load_lds_dwordx4 v208, s[44:45]
	s_add_u32 m0, s99, 0x4c80
	ds_read_b64_tr_b16 v[186:187], v212 offset:61568
	ds_read_b64_tr_b16 v[188:189], v212 offset:62592
	v_mfma_f32_16x16x32_bf16 v[32:35], v[178:181], v[140:143], v[32:35]
	global_load_lds_dwordx4 v209, s[44:45]
	s_add_u32 s28, s28, 0x80
	s_addc_u32 s29, s29, 0
	s_add_u32 s44, s44, 0x20000
	s_addc_u32 s45, s45, 0
	ds_read_b128 v[136:139], v211 offset:45120
	s_waitcnt lgkmcnt(6)
	v_mfma_f32_16x16x32_bf16 v[36:39], v[166:169], v[158:161], v[36:39]
	ds_read_b64_tr_b16 v[190:191], v213 offset:61568
	ds_read_b64_tr_b16 v[192:193], v213 offset:62592
	v_mfma_f32_16x16x32_bf16 v[40:43], v[170:173], v[158:161], v[40:43]
	ds_read_b64_tr_b16 v[198:199], v214 offset:61568
	ds_read_b64_tr_b16 v[200:201], v214 offset:62592
	v_mfma_f32_16x16x32_bf16 v[44:47], v[174:177], v[158:161], v[44:47]
	v_mfma_f32_16x16x32_bf16 v[48:51], v[178:181], v[158:161], v[48:51]
	ds_read_b128 v[140:143], v211 offset:46144
	s_waitcnt lgkmcnt(10)
	v_mfma_f32_16x16x32_bf16 v[52:55], v[166:169], v[162:165], v[52:55]
	v_mfma_f32_16x16x32_bf16 v[56:59], v[170:173], v[162:165], v[56:59]
	v_mfma_f32_16x16x32_bf16 v[60:63], v[174:177], v[162:165], v[60:63]
	v_mfma_f32_16x16x32_bf16 v[64:67], v[178:181], v[162:165], v[64:67]
	ds_read_b128 v[158:161], v211 offset:47168
	s_waitcnt lgkmcnt(6)
	v_mfma_f32_16x16x32_bf16 v[4:7], v[182:185], v[136:139], v[4:7]
	v_mfma_f32_16x16x32_bf16 v[8:11], v[186:189], v[136:139], v[8:11]
	s_waitcnt lgkmcnt(4)
	v_mfma_f32_16x16x32_bf16 v[12:15], v[190:193], v[136:139], v[12:15]
	s_waitcnt lgkmcnt(2)
	v_mfma_f32_16x16x32_bf16 v[16:19], v[198:201], v[136:139], v[16:19]
	ds_read_b128 v[162:165], v211 offset:48192
	s_waitcnt lgkmcnt(2)
	v_mfma_f32_16x16x32_bf16 v[20:23], v[182:185], v[140:143], v[20:23]
	v_mfma_f32_16x16x32_bf16 v[24:27], v[186:189], v[140:143], v[24:27]
	v_mfma_f32_16x16x32_bf16 v[28:31], v[190:193], v[140:143], v[28:31]
	v_mfma_f32_16x16x32_bf16 v[32:35], v[198:201], v[140:143], v[32:35]
	s_waitcnt lgkmcnt(1)
	v_mfma_f32_16x16x32_bf16 v[36:39], v[182:185], v[158:161], v[36:39]
	v_mfma_f32_16x16x32_bf16 v[40:43], v[186:189], v[158:161], v[40:43]
	v_mfma_f32_16x16x32_bf16 v[44:47], v[190:193], v[158:161], v[44:47]
	v_mfma_f32_16x16x32_bf16 v[48:51], v[198:201], v[158:161], v[48:51]
	s_waitcnt lgkmcnt(0)
	v_mfma_f32_16x16x32_bf16 v[52:55], v[182:185], v[162:165], v[52:55]
	v_mfma_f32_16x16x32_bf16 v[56:59], v[186:189], v[162:165], v[56:59]
	v_mfma_f32_16x16x32_bf16 v[60:63], v[190:193], v[162:165], v[60:63]
	v_mfma_f32_16x16x32_bf16 v[64:67], v[198:201], v[162:165], v[64:67]
	s_waitcnt vmcnt(0) lgkmcnt(0)
	s_barrier
	s_add_i32 s6, s6, 2
	s_cmp_lt_u32 s6, 6
	s_cbranch_scc1 .Lm2_loop
; #define LAS __attribute__((address_space(3)))
; __device__ __forceinline__ s16x4 lds_tr(lds_cptr p) { return __builtin_bit_cast(s16x4, __builtin_amdgcn_ds_read_tr16_b64_v4i16((LAS s16x4*)p)); }
;     ...
;     auto compute = [&]() __attribute__((always_inline)) {
; #pragma unroll
;         for (int kh = 0; kh < 2; ++kh) {
;             bf16x8 af[4], bfr[4];
; #pragma unroll
;             for (int m = 0; m < 4; ++m) af[m] = *(const LAS bf16x8*)(la + kh * GA_KH + m * 1024);
; #pragma unroll
;             for (int n = 0; n < 4; ++n) {
;                 const s16x4 r0 = lds_tr(lb + kh * 32 * GB_ST + n * 32), r1 = lds_tr(lb + kh * 32 * GB_ST + n * 32 + bsw);
;                 bfr[n] = (bf16x8){r0[0], r0[1], r0[2], r0[3], r1[0], r1[1], r1[2], r1[3]};
;             }
; #pragma unroll
;             for (int m = 0; m < 4; ++m)
; #pragma unroll
;                 for (int n = 0; n < 4; ++n) acc[m][n] = __builtin_amdgcn_mfma_f32_16x16x32_bf16(bfr[n], af[m], acc[m][n], 0, 0, 0);
;         }
;     };
;     ...
;     gloadB(0, rb0); gloadA(0, ra0); gloadB(1, rb1);
;     for (int kt = 0; kt < nk; kt += 2) {
;         __syncthreads();
;         lstore(ra0, rb0);
;         __syncthreads();
;         gloadA(kt + 1, ra0);
;         if (kt + 2 < nk) gloadB(kt + 2, rb0);
;         compute();
;         __syncthreads();
;         lstore(ra0, rb1);
;         __syncthreads();
;         if (kt + 2 < nk) gloadA(kt + 2, ra0);
;         if (kt + 3 < nk) gloadB(kt + 3, rb1);
;         compute();
;     }
	s_add_u32 m0, s98, 0x9000
	ds_read_b64_tr_b16 v[166:167], v210 offset:16512
	ds_read_b64_tr_b16 v[168:169], v210 offset:17536
	ds_read_b128 v[136:139], v211
	ds_read_b64_tr_b16 v[170:171], v212 offset:16512
	ds_read_b64_tr_b16 v[172:173], v212 offset:17536
	s_waitcnt lgkmcnt(2)
	v_mfma_f32_16x16x32_bf16 v[4:7], v[166:169], v[136:139], v[4:7]
	global_load_lds_dwordx4 v202, s[28:29]
	s_add_u32 m0, s98, 0xb040
	ds_read_b64_tr_b16 v[174:175], v213 offset:16512
	ds_read_b64_tr_b16 v[176:177], v213 offset:17536
	s_waitcnt lgkmcnt(2)
	v_mfma_f32_16x16x32_bf16 v[8:11], v[170:173], v[136:139], v[8:11]
	global_load_lds_dwordx4 v203, s[28:29]
	s_add_u32 m0, s98, 0x9400
	ds_read_b64_tr_b16 v[178:179], v214 offset:16512
	ds_read_b64_tr_b16 v[180:181], v214 offset:17536
	s_waitcnt lgkmcnt(2)
	v_mfma_f32_16x16x32_bf16 v[12:15], v[174:177], v[136:139], v[12:15]
	global_load_lds_dwordx4 v204, s[28:29]
	s_add_u32 m0, s98, 0xb440
	ds_read_b128 v[140:143], v211 offset:1024
	s_waitcnt lgkmcnt(1)
	v_mfma_f32_16x16x32_bf16 v[16:19], v[178:181], v[136:139], v[16:19]
	global_load_lds_dwordx4 v205, s[28:29]
	s_add_u32 m0, s99, 0xd080
	ds_read_b128 v[158:161], v211 offset:2048
	s_waitcnt lgkmcnt(1)
	v_mfma_f32_16x16x32_bf16 v[20:23], v[166:169], v[140:143], v[20:23]
	global_load_lds_dwordx4 v206, s[44:45]
	s_add_u32 m0, s99, 0xd480
	ds_read_b128 v[162:165], v211 offset:3072
	v_mfma_f32_16x16x32_bf16 v[24:27], v[170:173], v[140:143], v[24:27]
	global_load_lds_dwordx4 v207, s[44:45]
	s_add_u32 m0, s99, 0xd880
	ds_read_b64_tr_b16 v[182:183], v210 offset:24704
	ds_read_b64_tr_b16 v[184:185], v210 offset:25728
	v_mfma_f32_16x16x32_bf16 v[28:31], v[174:177], v[140:143], v[28:31]
	global_load_lds_dwordx4 v208, s[44:45]
	s_add_u32 m0, s99, 0xdc80
	ds_read_b64_tr_b16 v[186:187], v212 offset:24704
	ds_read_b64_tr_b16 v[188:189], v212 offset:25728
	v_mfma_f32_16x16x32_bf16 v[32:35], v[178:181], v[140:143], v[32:35]
	global_load_lds_dwordx4 v209, s[44:45]
	s_add_u32 s28, s28, 0x80
	s_addc_u32 s29, s29, 0
	s_add_u32 s44, s44, 0x20000
	s_addc_u32 s45, s45, 0
	ds_read_b128 v[136:139], v211 offset:8256
	s_waitcnt lgkmcnt(6)
	v_mfma_f32_16x16x32_bf16 v[36:39], v[166:169], v[158:161], v[36:39]
	ds_read_b64_tr_b16 v[190:191], v213 offset:24704
	ds_read_b64_tr_b16 v[192:193], v213 offset:25728
	v_mfma_f32_16x16x32_bf16 v[40:43], v[170:173], v[158:161], v[40:43]
	ds_read_b64_tr_b16 v[198:199], v214 offset:24704
	ds_read_b64_tr_b16 v[200:201], v214 offset:25728
	v_mfma_f32_16x16x32_bf16 v[44:47], v[174:177], v[158:161], v[44:47]
	v_mfma_f32_16x16x32_bf16 v[48:51], v[178:181], v[158:161], v[48:51]
	ds_read_b128 v[140:143], v211 offset:9280
	s_waitcnt lgkmcnt(10)
	v_mfma_f32_16x16x32_bf16 v[52:55], v[166:169], v[162:165], v[52:55]
	v_mfma_f32_16x16x32_bf16 v[56:59], v[170:173], v[162:165], v[56:59]
	v_mfma_f32_16x16x32_bf16 v[60:63], v[174:177], v[162:165], v[60:63]
	v_mfma_f32_16x16x32_bf16 v[64:67], v[178:181], v[162:165], v[64:67]
	ds_read_b128 v[158:161], v211 offset:10304
	s_waitcnt lgkmcnt(6)
	v_mfma_f32_16x16x32_bf16 v[4:7], v[182:185], v[136:139], v[4:7]
	v_mfma_f32_16x16x32_bf16 v[8:11], v[186:189], v[136:139], v[8:11]
	s_waitcnt lgkmcnt(4)
	v_mfma_f32_16x16x32_bf16 v[12:15], v[190:193], v[136:139], v[12:15]
	s_waitcnt lgkmcnt(2)
	v_mfma_f32_16x16x32_bf16 v[16:19], v[198:201], v[136:139], v[16:19]
	ds_read_b128 v[162:165], v211 offset:11328
	s_waitcnt lgkmcnt(2)
	v_mfma_f32_16x16x32_bf16 v[20:23], v[182:185], v[140:143], v[20:23]
	v_mfma_f32_16x16x32_bf16 v[24:27], v[186:189], v[140:143], v[24:27]
	v_mfma_f32_16x16x32_bf16 v[28:31], v[190:193], v[140:143], v[28:31]
	v_mfma_f32_16x16x32_bf16 v[32:35], v[198:201], v[140:143], v[32:35]
	s_waitcnt lgkmcnt(1)
	v_mfma_f32_16x16x32_bf16 v[36:39], v[182:185], v[158:161], v[36:39]
	v_mfma_f32_16x16x32_bf16 v[40:43], v[186:189], v[158:161], v[40:43]
	v_mfma_f32_16x16x32_bf16 v[44:47], v[190:193], v[158:161], v[44:47]
	v_mfma_f32_16x16x32_bf16 v[48:51], v[198:201], v[158:161], v[48:51]
	s_waitcnt lgkmcnt(0)
	v_mfma_f32_16x16x32_bf16 v[52:55], v[182:185], v[162:165], v[52:55]
	v_mfma_f32_16x16x32_bf16 v[56:59], v[186:189], v[162:165], v[56:59]
	v_mfma_f32_16x16x32_bf16 v[60:63], v[190:193], v[162:165], v[60:63]
	v_mfma_f32_16x16x32_bf16 v[64:67], v[198:201], v[162:165], v[64:67]
	s_waitcnt vmcnt(0) lgkmcnt(0)
	s_barrier
; #define LAS __attribute__((address_space(3)))
; __device__ __forceinline__ unsigned pk2bf(float lo, float hi) { const f32x2 v = {lo, hi}; return __builtin_bit_cast(unsigned, __builtin_convertvector(v, bf16x2_t)); }
;     template <class T> __device__ __forceinline__ T* w(size_t off) const { return (T*)(p->ws + off); }
; __device__ __forceinline__ s16x4 lds_tr(lds_cptr p) { return __builtin_bit_cast(s16x4, __builtin_amdgcn_ds_read_tr16_b64_v4i16((LAS s16x4*)p)); }
;     ...
;     auto compute = [&]() __attribute__((always_inline)) {
; #pragma unroll
;         for (int kh = 0; kh < 2; ++kh) {
;             bf16x8 af[4], bfr[4];
; #pragma unroll
;             for (int m = 0; m < 4; ++m) af[m] = *(const LAS bf16x8*)(la + kh * GA_KH + m * 1024);
; #pragma unroll
;             for (int n = 0; n < 4; ++n) {
;                 const s16x4 r0 = lds_tr(lb + kh * 32 * GB_ST + n * 32), r1 = lds_tr(lb + kh * 32 * GB_ST + n * 32 + bsw);
;                 bfr[n] = (bf16x8){r0[0], r0[1], r0[2], r0[3], r1[0], r1[1], r1[2], r1[3]};
;             }
; #pragma unroll
;             for (int m = 0; m < 4; ++m)
; #pragma unroll
;                 for (int n = 0; n < 4; ++n) acc[m][n] = __builtin_amdgcn_mfma_f32_16x16x32_bf16(bfr[n], af[m], acc[m][n], 0, 0, 0);
;         }
;     };
; __device__ __forceinline__ void ph_moe2_mfma(const Ctx& c, int layer, int tile, const int* sm, unsigned char* lds) {
;     ...
;     bf16* OUT = c.w<bf16>(WS_OUT);
; #pragma unroll
;     for (int m = 0; m < 4; ++m)
; #pragma unroll
;         for (int n = 0; n < 4; ++n) {
;             const int rl = wr * 64 + m * 16 + fr, col = nt * 128 + wc * 64 + n * 16 + fq * 4;
;             uint2 o; o.x = pk2bf(acc[m][n][0], acc[m][n][1]); o.y = pk2bf(acc[m][n][2], acc[m][n][3]);
;             *(uint2*)(OUT + (size_t)(s0 + rl) * D + col) = o;
;         }
	ds_read_b64_tr_b16 v[166:167], v210 offset:53376
	ds_read_b64_tr_b16 v[168:169], v210 offset:54400
	ds_read_b128 v[136:139], v211 offset:36864
	ds_read_b64_tr_b16 v[170:171], v212 offset:53376
	ds_read_b64_tr_b16 v[172:173], v212 offset:54400
	s_waitcnt lgkmcnt(2)
	v_mfma_f32_16x16x32_bf16 v[4:7], v[166:169], v[136:139], v[4:7]
	ds_read_b64_tr_b16 v[174:175], v213 offset:53376
	ds_read_b64_tr_b16 v[176:177], v213 offset:54400
	s_waitcnt lgkmcnt(2)
	v_mfma_f32_16x16x32_bf16 v[8:11], v[170:173], v[136:139], v[8:11]
	ds_read_b64_tr_b16 v[178:179], v214 offset:53376
	ds_read_b64_tr_b16 v[180:181], v214 offset:54400
	s_waitcnt lgkmcnt(2)
	v_mfma_f32_16x16x32_bf16 v[12:15], v[174:177], v[136:139], v[12:15]
	ds_read_b128 v[140:143], v211 offset:37888
	s_waitcnt lgkmcnt(1)
	v_mfma_f32_16x16x32_bf16 v[16:19], v[178:181], v[136:139], v[16:19]
	ds_read_b128 v[158:161], v211 offset:38912
	s_waitcnt lgkmcnt(1)
	v_mfma_f32_16x16x32_bf16 v[20:23], v[166:169], v[140:143], v[20:23]
	ds_read_b128 v[162:165], v211 offset:39936
	v_mfma_f32_16x16x32_bf16 v[24:27], v[170:173], v[140:143], v[24:27]
	ds_read_b64_tr_b16 v[182:183], v210 offset:61568
	ds_read_b64_tr_b16 v[184:185], v210 offset:62592
	v_mfma_f32_16x16x32_bf16 v[28:31], v[174:177], v[140:143], v[28:31]
	ds_read_b64_tr_b16 v[186:187], v212 offset:61568
	ds_read_b64_tr_b16 v[188:189], v212 offset:62592
	v_mfma_f32_16x16x32_bf16 v[32:35], v[178:181], v[140:143], v[32:35]
	ds_read_b128 v[136:139], v211 offset:45120
	s_waitcnt lgkmcnt(6)
	v_mfma_f32_16x16x32_bf16 v[36:39], v[166:169], v[158:161], v[36:39]
	ds_read_b64_tr_b16 v[190:191], v213 offset:61568
	ds_read_b64_tr_b16 v[192:193], v213 offset:62592
	v_mfma_f32_16x16x32_bf16 v[40:43], v[170:173], v[158:161], v[40:43]
	ds_read_b64_tr_b16 v[198:199], v214 offset:61568
	ds_read_b64_tr_b16 v[200:201], v214 offset:62592
	v_mfma_f32_16x16x32_bf16 v[44:47], v[174:177], v[158:161], v[44:47]
	v_mfma_f32_16x16x32_bf16 v[48:51], v[178:181], v[158:161], v[48:51]
	ds_read_b128 v[140:143], v211 offset:46144
	s_waitcnt lgkmcnt(10)
	v_mfma_f32_16x16x32_bf16 v[52:55], v[166:169], v[162:165], v[52:55]
	v_mfma_f32_16x16x32_bf16 v[56:59], v[170:173], v[162:165], v[56:59]
	v_mfma_f32_16x16x32_bf16 v[60:63], v[174:177], v[162:165], v[60:63]
	v_mfma_f32_16x16x32_bf16 v[64:67], v[178:181], v[162:165], v[64:67]
	ds_read_b128 v[158:161], v211 offset:47168
	s_waitcnt lgkmcnt(6)
	v_mfma_f32_16x16x32_bf16 v[4:7], v[182:185], v[136:139], v[4:7]
	v_mfma_f32_16x16x32_bf16 v[8:11], v[186:189], v[136:139], v[8:11]
	s_waitcnt lgkmcnt(4)
	v_mfma_f32_16x16x32_bf16 v[12:15], v[190:193], v[136:139], v[12:15]
	s_waitcnt lgkmcnt(2)
	v_mfma_f32_16x16x32_bf16 v[16:19], v[198:201], v[136:139], v[16:19]
	ds_read_b128 v[162:165], v211 offset:48192
	s_waitcnt lgkmcnt(2)
	v_mfma_f32_16x16x32_bf16 v[20:23], v[182:185], v[140:143], v[20:23]
	v_mfma_f32_16x16x32_bf16 v[24:27], v[186:189], v[140:143], v[24:27]
	v_mfma_f32_16x16x32_bf16 v[28:31], v[190:193], v[140:143], v[28:31]
	v_mfma_f32_16x16x32_bf16 v[32:35], v[198:201], v[140:143], v[32:35]
	s_waitcnt lgkmcnt(1)
	v_mfma_f32_16x16x32_bf16 v[36:39], v[182:185], v[158:161], v[36:39]
	v_mfma_f32_16x16x32_bf16 v[40:43], v[186:189], v[158:161], v[40:43]
	v_mfma_f32_16x16x32_bf16 v[44:47], v[190:193], v[158:161], v[44:47]
	v_mfma_f32_16x16x32_bf16 v[48:51], v[198:201], v[158:161], v[48:51]
	s_waitcnt lgkmcnt(0)
	v_mfma_f32_16x16x32_bf16 v[52:55], v[182:185], v[162:165], v[52:55]
	v_mfma_f32_16x16x32_bf16 v[56:59], v[186:189], v[162:165], v[56:59]
	v_mfma_f32_16x16x32_bf16 v[60:63], v[190:193], v[162:165], v[60:63]
	v_mfma_f32_16x16x32_bf16 v[64:67], v[198:201], v[162:165], v[64:67]
	s_waitcnt vmcnt(0) lgkmcnt(0)
	s_barrier
	s_lshl_b64 s[16:17], s[72:73], 11
	s_add_u32 s16, s42, s16
	s_addc_u32 s17, s43, s17
	s_add_u32 s16, s16, 0x67c6000
	s_addc_u32 s17, s17, 0
	s_lshl_b32 s6, s59, 8
	s_and_b32 s6, s6, 0x700
	s_add_u32 s16, s16, s6
	s_addc_u32 s17, s17, 0
	v_lshrrev_b32_e32 v217, 7, v118
	v_lshlrev_b32_e32 v217, 6, v217
	v_and_b32_e32 v215, 15, v118
	v_or_b32_e32 v217, v217, v215
	v_lshlrev_b32_e32 v217, 11, v217
	v_bfe_u32 v215, v118, 6, 1
	v_lshlrev_b32_e32 v215, 7, v215
	v_or_b32_e32 v217, v217, v215
	v_bfe_u32 v215, v118, 4, 2
	v_lshlrev_b32_e32 v215, 3, v215
	v_or_b32_e32 v217, v217, v215
	v_cvt_pk_bf16_f32 v218, v4, v5
	v_cvt_pk_bf16_f32 v219, v6, v7
	global_store_dwordx2 v217, v[218:219], s[16:17]
	s_nop 1
	v_cvt_pk_bf16_f32 v218, v8, v9
	v_cvt_pk_bf16_f32 v219, v10, v11
	global_store_dwordx2 v217, v[218:219], s[16:17] offset:32
	s_nop 1
	v_cvt_pk_bf16_f32 v218, v12, v13
	v_cvt_pk_bf16_f32 v219, v14, v15
	global_store_dwordx2 v217, v[218:219], s[16:17] offset:64
	s_nop 1
	v_cvt_pk_bf16_f32 v218, v16, v17
	v_cvt_pk_bf16_f32 v219, v18, v19
	global_store_dwordx2 v217, v[218:219], s[16:17] offset:96
	s_nop 1
	s_add_u32 s16, s16, 0x8000
	s_addc_u32 s17, s17, 0
	v_cvt_pk_bf16_f32 v218, v20, v21
	v_cvt_pk_bf16_f32 v219, v22, v23
	global_store_dwordx2 v217, v[218:219], s[16:17]
	s_nop 1
	v_cvt_pk_bf16_f32 v218, v24, v25
	v_cvt_pk_bf16_f32 v219, v26, v27
	global_store_dwordx2 v217, v[218:219], s[16:17] offset:32
	s_nop 1
	v_cvt_pk_bf16_f32 v218, v28, v29
	v_cvt_pk_bf16_f32 v219, v30, v31
	global_store_dwordx2 v217, v[218:219], s[16:17] offset:64
	s_nop 1
	v_cvt_pk_bf16_f32 v218, v32, v33
	v_cvt_pk_bf16_f32 v219, v34, v35
	global_store_dwordx2 v217, v[218:219], s[16:17] offset:96
	s_nop 1
	s_add_u32 s16, s16, 0x8000
	s_addc_u32 s17, s17, 0
	v_cvt_pk_bf16_f32 v218, v36, v37
	v_cvt_pk_bf16_f32 v219, v38, v39
	global_store_dwordx2 v217, v[218:219], s[16:17]
	s_nop 1
	v_cvt_pk_bf16_f32 v218, v40, v41
	v_cvt_pk_bf16_f32 v219, v42, v43
	global_store_dwordx2 v217, v[218:219], s[16:17] offset:32
	s_nop 1
	v_cvt_pk_bf16_f32 v218, v44, v45
	v_cvt_pk_bf16_f32 v219, v46, v47
	global_store_dwordx2 v217, v[218:219], s[16:17] offset:64
	s_nop 1
	v_cvt_pk_bf16_f32 v218, v48, v49
	v_cvt_pk_bf16_f32 v219, v50, v51
	global_store_dwordx2 v217, v[218:219], s[16:17] offset:96
	s_nop 1
	s_add_u32 s16, s16, 0x8000
	s_addc_u32 s17, s17, 0
	v_cvt_pk_bf16_f32 v218, v52, v53
	v_cvt_pk_bf16_f32 v219, v54, v55
	global_store_dwordx2 v217, v[218:219], s[16:17]
	s_nop 1
	v_cvt_pk_bf16_f32 v218, v56, v57
	v_cvt_pk_bf16_f32 v219, v58, v59
	global_store_dwordx2 v217, v[218:219], s[16:17] offset:32
	s_nop 1
	v_cvt_pk_bf16_f32 v218, v60, v61
	v_cvt_pk_bf16_f32 v219, v62, v63
	global_store_dwordx2 v217, v[218:219], s[16:17] offset:64
	s_nop 1
	v_cvt_pk_bf16_f32 v218, v64, v65
	v_cvt_pk_bf16_f32 v219, v66, v67
	global_store_dwordx2 v217, v[218:219], s[16:17] offset:96
	s_nop 1
